# P5 unit tail: heads 4..7 re-read requested before the first batch's stores (no vmcnt(0) between the two rescale batches)
# baseline (speedup 1.0000x reference)
.LBB0_544:
	v_readlane_b32 s2, v255, 58
	s_lshl_b32 s0, s2, 2
	s_mov_b32 s1, s3
	v_lshl_add_u64 v[54:55], v[168:169], 0, s[0:1]
	global_load_dwordx4 v[60:63], v[54:55], off
	global_load_dwordx4 v[64:67], v[54:55], off offset:64
	global_load_dwordx4 v[68:71], v[54:55], off offset:128
	global_load_dwordx4 v[72:75], v[54:55], off offset:192
	v_add_u32_e32 v6, s50, v232
	v_ashrrev_i32_e32 v7, 31, v6
	ds_read_b128 v[76:79], v159 offset:16384
	ds_read_b128 v[80:83], v159 offset:24576
	ds_read_b128 v[84:87], v159 offset:8192
	ds_read_b128 v[50:53], v159 offset:32768
	ds_read_b128 v[38:41], v214
	ds_read_b128 v[26:29], v214 offset:8192
	ds_read_b128 v[14:17], v214 offset:16384
	ds_read_b128 v[2:5], v214 offset:24576
	v_lshlrev_b64 v[56:57], 13, v[6:7]
	global_load_dwordx4 v[88:91], v[54:55], off offset:256
	global_load_dwordx4 v[92:95], v[54:55], off offset:320
	global_load_dwordx4 v[96:99], v[54:55], off offset:384
	global_load_dwordx4 v[100:103], v[54:55], off offset:448
	global_load_dwordx4 v[46:49], v[54:55], off offset:512
	global_load_dwordx4 v[42:45], v[54:55], off offset:576
	global_load_dwordx4 v[34:37], v[54:55], off offset:640
	global_load_dwordx4 v[30:33], v[54:55], off offset:704
	global_load_dwordx4 v[22:25], v[54:55], off offset:768
	global_load_dwordx4 v[18:21], v[54:55], off offset:832
	global_load_dwordx4 v[10:13], v[54:55], off offset:896
	global_load_dwordx4 v[6:9], v[54:55], off offset:960
	ds_bpermute_b32 v1, v240, v140
	v_readlane_b32 s0, v253, 57
	v_readlane_b32 s1, v253, 58
	s_waitcnt lgkmcnt(6)
	v_lshlrev_b32_e32 v104, 16, v84
	v_and_b32_e32 v84, 0xffff0000, v84
	s_waitcnt lgkmcnt(0)
	v_add_f32_e32 v1, v140, v1
	ds_bpermute_b32 v107, v241, v1
	v_lshl_add_u64 v[58:59], s[0:1], 0, v[56:57]
	s_mov_b32 s0, 0x800000
	v_lshlrev_b32_e32 v105, 16, v85
	v_and_b32_e32 v85, 0xffff0000, v85
	s_waitcnt lgkmcnt(0)
	v_add_f32_e32 v1, v1, v107
	v_fmamk_f32 v1, v1, 0x3b000000, v250
	v_mul_f32_e32 v107, 0x4b800000, v1
	v_cmp_gt_f32_e32 vcc, s0, v1
	v_mov_b32_e32 v173, v161
	v_lshlrev_b32_e32 v106, 16, v86
	v_cndmask_b32_e32 v1, v1, v107, vcc
	v_rsq_f32_e32 v1, v1
	v_and_b32_e32 v86, 0xffff0000, v86
	v_lshlrev_b32_e32 v108, 16, v87
	v_and_b32_e32 v87, 0xffff0000, v87
	v_mul_f32_e32 v110, 0x45800000, v1
	v_cndmask_b32_e32 v1, v1, v110, vcc
	v_mul_f32_e32 v104, v1, v104
	v_mul_f32_e32 v84, v1, v84
	v_mul_f32_e32 v105, v1, v105
	v_mul_f32_e32 v85, v1, v85
	s_lshl_b32 s2, s2, 1
	v_lshl_add_u64 v[56:57], v[58:59], 0, v[172:173]
	v_mul_f32_e32 v106, v1, v106
	v_mul_f32_e32 v86, v1, v86
	v_mul_f32_e32 v108, v1, v108
	v_mul_f32_e32 v87, v1, v87
	v_lshl_add_u64 v[56:57], v[56:57], 0, s[2:3]
	s_waitcnt vmcnt(16)
	global_load_dwordx4 v[112:115], v[56:57], off offset:512
	global_load_dwordx4 v[116:119], v[56:57], off offset:576
	global_load_dwordx4 v[120:123], v[56:57], off offset:640
	global_load_dwordx4 v[124:127], v[56:57], off offset:704
	global_load_dwordx4 v[128:131], v[56:57], off offset:768
	global_load_dwordx4 v[132:135], v[56:57], off offset:832
	global_load_dwordx4 v[136:139], v[56:57], off offset:896
	global_load_dwordx4 v[176:179], v[56:57], off offset:960
	v_lshlrev_b32_e32 v107, 16, v76
	v_and_b32_e32 v76, 0xffff0000, v76
	v_lshlrev_b32_e32 v109, 16, v77
	v_mul_f32_e32 v107, v1, v107
	v_mul_f32_e32 v76, v1, v76
	v_mul_f32_e32 v109, v1, v109
	v_readlane_b32 s83, v255, 57
	v_readlane_b32 s0, v255, 55
	s_add_i32 s49, s49, s83
	s_add_i32 s0, s0, s83
	v_writelane_b32 v255, s0, 55
	s_cmpk_lt_i32 s49, 0x400
	s_mov_b32 s84, s53
	s_mov_b64 s[86:87], s[54:55]
	s_mov_b32 s85, 0x41a00000
	s_waitcnt vmcnt(23)
	v_mul_f32_e32 v60, v60, v104
	v_mul_f32_e32 v61, v61, v84
	v_mul_f32_e32 v62, v62, v105
	v_mul_f32_e32 v63, v63, v85
	s_waitcnt vmcnt(22)
	v_mul_f32_e32 v64, v64, v106
	v_mul_f32_e32 v65, v65, v86
	v_mul_f32_e32 v66, v66, v108
	v_mul_f32_e32 v67, v67, v87
	v_cvt_pk_bf16_f32 v60, v60, v61
	v_cvt_pk_bf16_f32 v61, v62, v63
	v_cvt_pk_bf16_f32 v62, v64, v65
	v_cvt_pk_bf16_f32 v63, v66, v67
	global_store_dwordx4 v[56:57], v[60:63], off
	s_waitcnt vmcnt(22)
	v_mul_f32_e32 v68, v68, v107
	v_mul_f32_e32 v69, v69, v76
	v_and_b32_e32 v61, 0xffff0000, v77
	v_lshlrev_b32_e32 v62, 16, v78
	v_and_b32_e32 v63, 0xffff0000, v78
	v_mul_f32_e32 v61, v1, v61
	v_mul_f32_e32 v62, v1, v62
	v_mul_f32_e32 v63, v1, v63
	v_mul_f32_e32 v61, v71, v61
	s_waitcnt vmcnt(21)
	v_mul_f32_e32 v62, v72, v62
	v_mul_f32_e32 v63, v73, v63
	v_mul_f32_e32 v70, v70, v109
	v_cvt_pk_bf16_f32 v60, v68, v69
	v_cvt_pk_bf16_f32 v61, v70, v61
	v_cvt_pk_bf16_f32 v62, v62, v63
	v_lshlrev_b32_e32 v63, 16, v79
	v_mul_f32_e32 v63, v1, v63
	v_and_b32_e32 v64, 0xffff0000, v79
	v_mul_f32_e32 v63, v74, v63
	v_mul_f32_e32 v64, v1, v64
	v_mul_f32_e32 v64, v75, v64
	v_cvt_pk_bf16_f32 v63, v63, v64
	global_store_dwordx4 v[56:57], v[60:63], off offset:64
	v_and_b32_e32 v64, 0xffff0000, v83
	v_mul_f32_e32 v64, v1, v64
	v_lshlrev_b32_e32 v60, 16, v80
	v_and_b32_e32 v61, 0xffff0000, v80
	v_mul_f32_e32 v60, v1, v60
	v_mul_f32_e32 v61, v1, v61
	s_waitcnt vmcnt(21)
	v_mul_f32_e32 v60, v88, v60
	v_mul_f32_e32 v61, v89, v61
	v_cvt_pk_bf16_f32 v60, v60, v61
	v_lshlrev_b32_e32 v61, 16, v81
	v_and_b32_e32 v62, 0xffff0000, v81
	v_mul_f32_e32 v61, v1, v61
	v_mul_f32_e32 v62, v1, v62
	v_mul_f32_e32 v61, v90, v61
	v_mul_f32_e32 v62, v91, v62
	v_cvt_pk_bf16_f32 v61, v61, v62
	v_lshlrev_b32_e32 v62, 16, v82
	v_and_b32_e32 v63, 0xffff0000, v82
	v_mul_f32_e32 v62, v1, v62
	v_mul_f32_e32 v63, v1, v63
	s_waitcnt vmcnt(20)
	v_mul_f32_e32 v62, v92, v62
	v_mul_f32_e32 v63, v93, v63
	v_cvt_pk_bf16_f32 v62, v62, v63
	v_lshlrev_b32_e32 v63, 16, v83
	v_mul_f32_e32 v63, v1, v63
	v_mul_f32_e32 v63, v94, v63
	v_mul_f32_e32 v64, v95, v64
	v_cvt_pk_bf16_f32 v63, v63, v64
	global_store_dwordx4 v[56:57], v[60:63], off offset:128
	s_nop 1
	v_lshlrev_b32_e32 v60, 16, v50
	v_and_b32_e32 v50, 0xffff0000, v50
	v_mul_f32_e32 v60, v1, v60
	v_mul_f32_e32 v50, v1, v50
	s_waitcnt vmcnt(20)
	v_mul_f32_e32 v60, v96, v60
	v_mul_f32_e32 v50, v97, v50
	v_cvt_pk_bf16_f32 v50, v60, v50
	v_lshlrev_b32_e32 v60, 16, v51
	v_and_b32_e32 v51, 0xffff0000, v51
	v_mul_f32_e32 v60, v1, v60
	v_mul_f32_e32 v51, v1, v51
	v_mul_f32_e32 v60, v98, v60
	v_mul_f32_e32 v51, v99, v51
	v_cvt_pk_bf16_f32 v51, v60, v51
	v_lshlrev_b32_e32 v60, 16, v52
	v_and_b32_e32 v52, 0xffff0000, v52
	v_mul_f32_e32 v60, v1, v60
	v_mul_f32_e32 v52, v1, v52
	s_waitcnt vmcnt(19)
	v_mul_f32_e32 v60, v100, v60
	v_mul_f32_e32 v52, v101, v52
	v_cvt_pk_bf16_f32 v52, v60, v52
	v_lshlrev_b32_e32 v60, 16, v53
	v_and_b32_e32 v53, 0xffff0000, v53
	v_mul_f32_e32 v53, v1, v53
	v_mul_f32_e32 v60, v1, v60
	v_mul_f32_e32 v53, v103, v53
	v_mul_f32_e32 v60, v102, v60
	v_cvt_pk_bf16_f32 v53, v60, v53
	global_store_dwordx4 v[56:57], v[50:53], off offset:192
	s_nop 1
	v_lshlrev_b32_e32 v50, 16, v38
	v_and_b32_e32 v38, 0xffff0000, v38
	v_mul_f32_e32 v50, v1, v50
	v_mul_f32_e32 v38, v1, v38
	s_waitcnt vmcnt(19)
	v_mul_f32_e32 v46, v46, v50
	v_mul_f32_e32 v38, v47, v38
	v_cvt_pk_bf16_f32 v38, v46, v38
	v_lshlrev_b32_e32 v46, 16, v39
	v_and_b32_e32 v39, 0xffff0000, v39
	v_mul_f32_e32 v46, v1, v46
	v_mul_f32_e32 v39, v1, v39
	v_mul_f32_e32 v46, v48, v46
	v_mul_f32_e32 v39, v49, v39
	v_cvt_pk_bf16_f32 v39, v46, v39
	v_lshlrev_b32_e32 v46, 16, v40
	v_and_b32_e32 v40, 0xffff0000, v40
	v_mul_f32_e32 v46, v1, v46
	v_mul_f32_e32 v40, v1, v40
	s_waitcnt vmcnt(18)
	v_mul_f32_e32 v42, v42, v46
	v_mul_f32_e32 v40, v43, v40
	v_cvt_pk_bf16_f32 v40, v42, v40
	v_lshlrev_b32_e32 v42, 16, v41
	v_and_b32_e32 v41, 0xffff0000, v41
	v_mul_f32_e32 v41, v1, v41
	v_mul_f32_e32 v42, v1, v42
	v_mul_f32_e32 v41, v45, v41
	v_mul_f32_e32 v42, v44, v42
	v_cvt_pk_bf16_f32 v41, v42, v41
	global_store_dwordx4 v[56:57], v[38:41], off offset:256
	s_nop 1
	v_lshlrev_b32_e32 v38, 16, v26
	v_and_b32_e32 v26, 0xffff0000, v26
	v_mul_f32_e32 v38, v1, v38
	v_mul_f32_e32 v26, v1, v26
	s_waitcnt vmcnt(18)
	v_mul_f32_e32 v34, v34, v38
	v_mul_f32_e32 v26, v35, v26
	v_cvt_pk_bf16_f32 v26, v34, v26
	v_lshlrev_b32_e32 v34, 16, v27
	v_and_b32_e32 v27, 0xffff0000, v27
	v_mul_f32_e32 v34, v1, v34
	v_mul_f32_e32 v27, v1, v27
	v_mul_f32_e32 v34, v36, v34
	v_mul_f32_e32 v27, v37, v27
	v_cvt_pk_bf16_f32 v27, v34, v27
	v_lshlrev_b32_e32 v34, 16, v28
	v_and_b32_e32 v28, 0xffff0000, v28
	v_mul_f32_e32 v34, v1, v34
	v_mul_f32_e32 v28, v1, v28
	s_waitcnt vmcnt(17)
	v_mul_f32_e32 v30, v30, v34
	v_mul_f32_e32 v28, v31, v28
	v_cvt_pk_bf16_f32 v28, v30, v28
	v_lshlrev_b32_e32 v30, 16, v29
	v_and_b32_e32 v29, 0xffff0000, v29
	v_mul_f32_e32 v29, v1, v29
	v_mul_f32_e32 v30, v1, v30
	v_mul_f32_e32 v29, v33, v29
	v_mul_f32_e32 v30, v32, v30
	v_cvt_pk_bf16_f32 v29, v30, v29
	global_store_dwordx4 v[56:57], v[26:29], off offset:320
	s_nop 1
	v_lshlrev_b32_e32 v26, 16, v14
	v_and_b32_e32 v14, 0xffff0000, v14
	v_mul_f32_e32 v26, v1, v26
	v_mul_f32_e32 v14, v1, v14
	s_waitcnt vmcnt(17)
	v_mul_f32_e32 v22, v22, v26
	v_mul_f32_e32 v14, v23, v14
	v_cvt_pk_bf16_f32 v14, v22, v14
	v_lshlrev_b32_e32 v22, 16, v15
	v_and_b32_e32 v15, 0xffff0000, v15
	v_mul_f32_e32 v22, v1, v22
	v_mul_f32_e32 v15, v1, v15
	v_mul_f32_e32 v22, v24, v22
	v_mul_f32_e32 v15, v25, v15
	v_cvt_pk_bf16_f32 v15, v22, v15
	v_lshlrev_b32_e32 v22, 16, v16
	v_and_b32_e32 v16, 0xffff0000, v16
	v_mul_f32_e32 v22, v1, v22
	v_mul_f32_e32 v16, v1, v16
	s_waitcnt vmcnt(16)
	v_mul_f32_e32 v18, v18, v22
	v_mul_f32_e32 v16, v19, v16
	v_cvt_pk_bf16_f32 v16, v18, v16
	v_lshlrev_b32_e32 v18, 16, v17
	v_and_b32_e32 v17, 0xffff0000, v17
	v_mul_f32_e32 v17, v1, v17
	v_mul_f32_e32 v18, v1, v18
	v_mul_f32_e32 v17, v21, v17
	v_mul_f32_e32 v18, v20, v18
	v_cvt_pk_bf16_f32 v17, v18, v17
	global_store_dwordx4 v[56:57], v[14:17], off offset:384
	s_nop 1
	v_lshlrev_b32_e32 v14, 16, v2
	v_and_b32_e32 v2, 0xffff0000, v2
	v_mul_f32_e32 v14, v1, v14
	v_mul_f32_e32 v2, v1, v2
	s_waitcnt vmcnt(16)
	v_mul_f32_e32 v10, v10, v14
	v_mul_f32_e32 v2, v11, v2
	v_cvt_pk_bf16_f32 v2, v10, v2
	v_lshlrev_b32_e32 v10, 16, v3
	v_and_b32_e32 v3, 0xffff0000, v3
	v_mul_f32_e32 v10, v1, v10
	v_mul_f32_e32 v3, v1, v3
	v_mul_f32_e32 v10, v12, v10
	v_mul_f32_e32 v3, v13, v3
	v_cvt_pk_bf16_f32 v3, v10, v3
	v_lshlrev_b32_e32 v10, 16, v4
	v_and_b32_e32 v4, 0xffff0000, v4
	v_mul_f32_e32 v10, v1, v10
	v_mul_f32_e32 v4, v1, v4
	s_waitcnt vmcnt(15)
	v_mul_f32_e32 v6, v6, v10
	v_mul_f32_e32 v4, v7, v4
	v_cvt_pk_bf16_f32 v4, v6, v4
	v_lshlrev_b32_e32 v6, 16, v5
	v_and_b32_e32 v5, 0xffff0000, v5
	v_mul_f32_e32 v5, v1, v5
	v_mul_f32_e32 v6, v1, v6
	v_mul_f32_e32 v5, v9, v5
	v_mul_f32_e32 v6, v8, v6
	v_cvt_pk_bf16_f32 v5, v6, v5
	global_store_dwordx4 v[56:57], v[2:5], off offset:448
	s_waitcnt vmcnt(8)
	v_mov_b64_e32 v[12:13], v[112:113]
	v_mov_b64_e32 v[14:15], v[114:115]
	global_load_dwordx4 v[16:19], v[54:55], off offset:1024
	global_load_dwordx4 v[20:23], v[54:55], off offset:1088
	v_mov_b64_e32 v[24:25], v[116:117]
	v_mov_b64_e32 v[26:27], v[118:119]
	global_load_dwordx4 v[28:31], v[54:55], off offset:1152
	global_load_dwordx4 v[32:35], v[54:55], off offset:1216
	v_mov_b64_e32 v[36:37], v[120:121]
	v_mov_b64_e32 v[38:39], v[122:123]
	global_load_dwordx4 v[40:43], v[54:55], off offset:1280
	v_lshl_add_u64 v[2:3], v[58:59], 0, s[2:3]
	v_lshl_add_u64 v[10:11], v[2:3], 0, v[172:173]
	global_load_dwordx4 v[44:47], v[54:55], off offset:1344
	global_load_dwordx4 v[48:51], v[54:55], off offset:1408
	global_load_dwordx4 v[58:61], v[54:55], off offset:1472
	v_mov_b64_e32 v[62:63], v[124:125]
	v_mov_b64_e32 v[64:65], v[126:127]
	global_load_dwordx4 v[66:69], v[54:55], off offset:1536
	global_load_dwordx4 v[70:73], v[54:55], off offset:1600
	global_load_dwordx4 v[74:77], v[54:55], off offset:1664
	global_load_dwordx4 v[78:81], v[54:55], off offset:1728
	v_mov_b64_e32 v[82:83], v[128:129]
	v_mov_b64_e32 v[84:85], v[130:131]
	v_mov_b64_e32 v[86:87], v[132:133]
	v_mov_b64_e32 v[88:89], v[134:135]
	global_load_dwordx4 v[90:93], v[54:55], off offset:1792
	global_load_dwordx4 v[94:97], v[54:55], off offset:1856
	global_load_dwordx4 v[98:101], v[54:55], off offset:1920
	global_load_dwordx4 v[2:5], v[54:55], off offset:1984
	s_nop 0
	v_mov_b64_e32 v[52:53], v[136:137]
	v_mov_b64_e32 v[54:55], v[138:139]
	v_mov_b64_e32 v[6:7], v[176:177]
	v_mov_b64_e32 v[8:9], v[178:179]
	s_waitcnt vmcnt(16)
	v_lshlrev_b32_e32 v56, 16, v12
	v_and_b32_e32 v12, 0xffff0000, v12
	v_mul_f32_e32 v56, v1, v56
	v_mul_f32_e32 v12, v1, v12
	s_waitcnt vmcnt(15)
	v_mul_f32_e32 v16, v16, v56
	v_mul_f32_e32 v12, v17, v12
	v_cvt_pk_bf16_f32 v12, v16, v12
	v_lshlrev_b32_e32 v16, 16, v13
	v_and_b32_e32 v13, 0xffff0000, v13
	v_mul_f32_e32 v16, v1, v16
	v_mul_f32_e32 v13, v1, v13
	v_mul_f32_e32 v16, v18, v16
	v_mul_f32_e32 v13, v19, v13
	v_cvt_pk_bf16_f32 v13, v16, v13
	v_lshlrev_b32_e32 v16, 16, v14
	v_and_b32_e32 v14, 0xffff0000, v14
	v_mul_f32_e32 v16, v1, v16
	v_mul_f32_e32 v14, v1, v14
	s_waitcnt vmcnt(14)
	v_mul_f32_e32 v16, v20, v16
	v_mul_f32_e32 v14, v21, v14
	v_cvt_pk_bf16_f32 v14, v16, v14
	v_lshlrev_b32_e32 v16, 16, v15
	v_and_b32_e32 v15, 0xffff0000, v15
	v_mul_f32_e32 v15, v1, v15
	v_mul_f32_e32 v16, v1, v16
	v_mul_f32_e32 v15, v23, v15
	v_mul_f32_e32 v16, v22, v16
	v_cvt_pk_bf16_f32 v15, v16, v15
	global_store_dwordx4 v[10:11], v[12:15], off offset:512
	s_waitcnt vmcnt(15)
	v_and_b32_e32 v16, 0xffff0000, v27
	v_mul_f32_e32 v16, v1, v16
	v_lshlrev_b32_e32 v12, 16, v24
	v_and_b32_e32 v13, 0xffff0000, v24
	v_mul_f32_e32 v12, v1, v12
	v_mul_f32_e32 v13, v1, v13
	s_waitcnt vmcnt(14)
	v_mul_f32_e32 v12, v28, v12
	v_mul_f32_e32 v13, v29, v13
	v_cvt_pk_bf16_f32 v12, v12, v13
	v_lshlrev_b32_e32 v13, 16, v25
	v_and_b32_e32 v14, 0xffff0000, v25
	v_mul_f32_e32 v13, v1, v13
	v_mul_f32_e32 v14, v1, v14
	v_mul_f32_e32 v13, v30, v13
	v_mul_f32_e32 v14, v31, v14
	v_cvt_pk_bf16_f32 v13, v13, v14
	v_lshlrev_b32_e32 v14, 16, v26
	v_and_b32_e32 v15, 0xffff0000, v26
	v_mul_f32_e32 v14, v1, v14
	v_mul_f32_e32 v15, v1, v15
	s_waitcnt vmcnt(13)
	v_mul_f32_e32 v14, v32, v14
	v_mul_f32_e32 v15, v33, v15
	v_cvt_pk_bf16_f32 v14, v14, v15
	v_lshlrev_b32_e32 v15, 16, v27
	v_mul_f32_e32 v15, v1, v15
	v_mul_f32_e32 v15, v34, v15
	v_mul_f32_e32 v16, v35, v16
	v_cvt_pk_bf16_f32 v15, v15, v16
	global_store_dwordx4 v[10:11], v[12:15], off offset:576
	s_waitcnt vmcnt(14)
	v_and_b32_e32 v16, 0xffff0000, v39
	v_mul_f32_e32 v16, v1, v16
	v_lshlrev_b32_e32 v12, 16, v36
	v_and_b32_e32 v13, 0xffff0000, v36
	v_mul_f32_e32 v12, v1, v12
	v_mul_f32_e32 v13, v1, v13
	s_waitcnt vmcnt(13)
	v_mul_f32_e32 v12, v40, v12
	v_mul_f32_e32 v13, v41, v13
	v_cvt_pk_bf16_f32 v12, v12, v13
	v_lshlrev_b32_e32 v13, 16, v37
	v_and_b32_e32 v14, 0xffff0000, v37
	v_mul_f32_e32 v13, v1, v13
	v_mul_f32_e32 v14, v1, v14
	v_mul_f32_e32 v13, v42, v13
	v_mul_f32_e32 v14, v43, v14
	v_cvt_pk_bf16_f32 v13, v13, v14
	v_lshlrev_b32_e32 v14, 16, v38
	v_and_b32_e32 v15, 0xffff0000, v38
	v_mul_f32_e32 v14, v1, v14
	v_mul_f32_e32 v15, v1, v15
	s_waitcnt vmcnt(12)
	v_mul_f32_e32 v14, v44, v14
	v_mul_f32_e32 v15, v45, v15
	v_cvt_pk_bf16_f32 v14, v14, v15
	v_lshlrev_b32_e32 v15, 16, v39
	v_mul_f32_e32 v15, v1, v15
	v_mul_f32_e32 v15, v46, v15
	v_mul_f32_e32 v16, v47, v16
	v_cvt_pk_bf16_f32 v15, v15, v16
	global_store_dwordx4 v[10:11], v[12:15], off offset:640
	s_waitcnt vmcnt(11)
	v_and_b32_e32 v16, 0xffff0000, v65
	v_mul_f32_e32 v16, v1, v16
	v_lshlrev_b32_e32 v12, 16, v62
	v_and_b32_e32 v13, 0xffff0000, v62
	v_mul_f32_e32 v12, v1, v12
	v_mul_f32_e32 v13, v1, v13
	v_mul_f32_e32 v12, v48, v12
	v_mul_f32_e32 v13, v49, v13
	v_cvt_pk_bf16_f32 v12, v12, v13
	v_lshlrev_b32_e32 v13, 16, v63
	v_and_b32_e32 v14, 0xffff0000, v63
	v_mul_f32_e32 v13, v1, v13
	v_mul_f32_e32 v14, v1, v14
	v_mul_f32_e32 v13, v50, v13
	v_mul_f32_e32 v14, v51, v14
	v_cvt_pk_bf16_f32 v13, v13, v14
	v_lshlrev_b32_e32 v14, 16, v64
	v_and_b32_e32 v15, 0xffff0000, v64
	v_mul_f32_e32 v14, v1, v14
	v_mul_f32_e32 v15, v1, v15
	v_mul_f32_e32 v14, v58, v14
	v_mul_f32_e32 v15, v59, v15
	v_cvt_pk_bf16_f32 v14, v14, v15
	v_lshlrev_b32_e32 v15, 16, v65
	v_mul_f32_e32 v15, v1, v15
	v_mul_f32_e32 v15, v60, v15
	v_mul_f32_e32 v16, v61, v16
	v_cvt_pk_bf16_f32 v15, v15, v16
	global_store_dwordx4 v[10:11], v[12:15], off offset:704
	s_waitcnt vmcnt(8)
	v_and_b32_e32 v16, 0xffff0000, v85
	v_mul_f32_e32 v16, v1, v16
	v_lshlrev_b32_e32 v12, 16, v82
	v_and_b32_e32 v13, 0xffff0000, v82
	v_mul_f32_e32 v12, v1, v12
	v_mul_f32_e32 v13, v1, v13
	v_mul_f32_e32 v12, v66, v12
	v_mul_f32_e32 v13, v67, v13
	v_cvt_pk_bf16_f32 v12, v12, v13
	v_lshlrev_b32_e32 v13, 16, v83
	v_and_b32_e32 v14, 0xffff0000, v83
	v_mul_f32_e32 v13, v1, v13
	v_mul_f32_e32 v14, v1, v14
	v_mul_f32_e32 v13, v68, v13
	v_mul_f32_e32 v14, v69, v14
	v_cvt_pk_bf16_f32 v13, v13, v14
	v_lshlrev_b32_e32 v14, 16, v84
	v_and_b32_e32 v15, 0xffff0000, v84
	v_mul_f32_e32 v14, v1, v14
	v_mul_f32_e32 v15, v1, v15
	v_mul_f32_e32 v14, v70, v14
	v_mul_f32_e32 v15, v71, v15
	v_cvt_pk_bf16_f32 v14, v14, v15
	v_lshlrev_b32_e32 v15, 16, v85
	v_mul_f32_e32 v15, v1, v15
	v_mul_f32_e32 v15, v72, v15
	v_mul_f32_e32 v16, v73, v16
	v_cvt_pk_bf16_f32 v15, v15, v16
	global_store_dwordx4 v[10:11], v[12:15], off offset:768
	s_waitcnt vmcnt(9)
	v_and_b32_e32 v16, 0xffff0000, v89
	v_mul_f32_e32 v16, v1, v16
	v_lshlrev_b32_e32 v12, 16, v86
	v_and_b32_e32 v13, 0xffff0000, v86
	v_mul_f32_e32 v12, v1, v12
	v_mul_f32_e32 v13, v1, v13
	v_mul_f32_e32 v12, v74, v12
	v_mul_f32_e32 v13, v75, v13
	v_cvt_pk_bf16_f32 v12, v12, v13
	v_lshlrev_b32_e32 v13, 16, v87
	v_and_b32_e32 v14, 0xffff0000, v87
	v_mul_f32_e32 v13, v1, v13
	v_mul_f32_e32 v14, v1, v14
	v_mul_f32_e32 v13, v76, v13
	v_mul_f32_e32 v14, v77, v14
	v_cvt_pk_bf16_f32 v13, v13, v14
	v_lshlrev_b32_e32 v14, 16, v88
	v_and_b32_e32 v15, 0xffff0000, v88
	v_mul_f32_e32 v14, v1, v14
	v_mul_f32_e32 v15, v1, v15
	v_mul_f32_e32 v14, v78, v14
	v_mul_f32_e32 v15, v79, v15
	v_cvt_pk_bf16_f32 v14, v14, v15
	v_lshlrev_b32_e32 v15, 16, v89
	v_mul_f32_e32 v15, v1, v15
	v_mul_f32_e32 v15, v80, v15
	v_mul_f32_e32 v16, v81, v16
	v_cvt_pk_bf16_f32 v15, v15, v16
	global_store_dwordx4 v[10:11], v[12:15], off offset:832
	s_waitcnt vmcnt(6)
	v_and_b32_e32 v16, 0xffff0000, v55
	v_mul_f32_e32 v16, v1, v16
	v_lshlrev_b32_e32 v12, 16, v52
	v_and_b32_e32 v13, 0xffff0000, v52
	v_mul_f32_e32 v12, v1, v12
	v_mul_f32_e32 v13, v1, v13
	v_mul_f32_e32 v12, v90, v12
	v_mul_f32_e32 v13, v91, v13
	v_cvt_pk_bf16_f32 v12, v12, v13
	v_lshlrev_b32_e32 v13, 16, v53
	v_and_b32_e32 v14, 0xffff0000, v53
	v_mul_f32_e32 v13, v1, v13
	v_mul_f32_e32 v14, v1, v14
	v_mul_f32_e32 v13, v92, v13
	v_mul_f32_e32 v14, v93, v14
	v_cvt_pk_bf16_f32 v13, v13, v14
	v_lshlrev_b32_e32 v14, 16, v54
	v_and_b32_e32 v15, 0xffff0000, v54
	v_mul_f32_e32 v14, v1, v14
	v_mul_f32_e32 v15, v1, v15
	v_mul_f32_e32 v14, v94, v14
	v_mul_f32_e32 v15, v95, v15
	v_cvt_pk_bf16_f32 v14, v14, v15
	v_lshlrev_b32_e32 v15, 16, v55
	v_mul_f32_e32 v15, v1, v15
	v_mul_f32_e32 v15, v96, v15
	v_mul_f32_e32 v16, v97, v16
	v_cvt_pk_bf16_f32 v15, v15, v16
	global_store_dwordx4 v[10:11], v[12:15], off offset:896
	s_waitcnt vmcnt(7)
	s_nop 0
	v_lshlrev_b32_e32 v12, 16, v6
	v_and_b32_e32 v6, 0xffff0000, v6
	v_mul_f32_e32 v12, v1, v12
	v_mul_f32_e32 v6, v1, v6
	v_mul_f32_e32 v12, v98, v12
	v_mul_f32_e32 v6, v99, v6
	v_cvt_pk_bf16_f32 v6, v12, v6
	v_lshlrev_b32_e32 v12, 16, v7
	v_and_b32_e32 v7, 0xffff0000, v7
	v_mul_f32_e32 v12, v1, v12
	v_mul_f32_e32 v7, v1, v7
	v_mul_f32_e32 v12, v100, v12
	v_mul_f32_e32 v7, v101, v7
	v_cvt_pk_bf16_f32 v7, v12, v7
	v_lshlrev_b32_e32 v12, 16, v8
	v_and_b32_e32 v8, 0xffff0000, v8
	v_mul_f32_e32 v12, v1, v12
	v_mul_f32_e32 v8, v1, v8
	v_mul_f32_e32 v2, v2, v12
	v_mul_f32_e32 v3, v3, v8
	v_cvt_pk_bf16_f32 v8, v2, v3
	v_lshlrev_b32_e32 v2, 16, v9
	v_and_b32_e32 v3, 0xffff0000, v9
	v_mul_f32_e32 v2, v1, v2
	v_mul_f32_e32 v1, v1, v3
	v_mul_f32_e32 v2, v4, v2
	v_mul_f32_e32 v1, v5, v1
	v_cvt_pk_bf16_f32 v9, v2, v1
	global_store_dwordx4 v[10:11], v[6:9], off offset:960
	s_cbranch_scc0 .LBB0_599
